# baseline (speedup 1.0000x reference)
.Lpf_skip:
	v_mov_b64_e32 v[18:19], s[8:9]
	v_mov_b64_e32 v[0:1], s[4:5]
	v_mov_b64_e32 v[16:17], v[20:21]
	s_and_saveexec_b64 s[2:3], vcc
	v_mov_b32_e32 v17, 0
	v_lshlrev_b64 v[0:1], 15, v[20:21]
	v_add_u32_e32 v1, -8, v1
	v_mov_b32_e32 v0, v17
	v_ashrrev_i64 v[0:1], 11, v[0:1]
	v_and_b32_e32 v16, 0x1ffff, v20
	v_lshl_add_u64 v[18:19], s[10:11], 0, v[0:1]
	v_mov_b64_e32 v[0:1], s[22:23]
	s_or_b64 exec, exec, s[2:3]
	v_lshlrev_b64 v[2:3], 5, v[16:17]
	v_lshl_add_u64 v[8:9], v[0:1], 0, v[2:3]
	global_load_dwordx4 v[0:3], v[8:9], off offset:16 nt sc1
	global_load_dwordx4 v[4:7], v[8:9], off nt sc1
	s_mov_b64 s[2:3], 0x80000
	v_lshl_add_u64 v[22:23], v[20:21], 0, s[2:3]
	v_cmp_lt_u64_e32 vcc, s[0:1], v[22:23]
	v_mov_b64_e32 v[8:9], s[4:5]
	v_mov_b64_e32 v[24:25], s[8:9]
	s_and_saveexec_b64 s[0:1], vcc
	s_cbranch_execz .LBB0_14
	s_mov_b32 s2, 0xfff80000
	s_mov_b32 s3, -1
	v_lshl_add_u64 v[10:11], v[20:21], 0, s[2:3]
	v_alignbit_b32 v12, v11, v10, 17
	v_cmp_lt_i32_e32 vcc, 0, v12
	s_mov_b64 s[2:3], 0
	s_and_saveexec_b64 s[6:7], vcc
	s_xor_b64 s[6:7], exec, s[6:7]
	s_cbranch_execz .LBB0_31
	v_cmp_eq_u32_e32 vcc, 1, v12
	s_mov_b64 s[2:3], -1
	s_and_saveexec_b64 s[14:15], vcc
	s_xor_b64 s[2:3], exec, -1
	s_or_b64 exec, exec, s[14:15]
	s_and_b64 s[2:3], s[2:3], exec
	s_or_saveexec_b64 s[6:7], s[6:7]
	v_mov_b64_e32 v[8:9], s[18:19]
	s_xor_b64 exec, exec, s[6:7]
	s_cbranch_execnz .LBB0_32

.LBB0_14:
	s_or_b64 exec, exec, s[0:1]
	v_lshlrev_b64 v[10:11], 5, v[22:23]
	v_lshl_add_u64 v[26:27], v[8:9], 0, v[10:11]
	global_load_dwordx4 v[8:11], v[26:27], off offset:16 nt sc1
	global_load_dwordx4 v[12:15], v[26:27], off nt sc1
	s_mov_b64 s[0:1], 0x100000
	v_lshl_add_u64 v[26:27], v[20:21], 0, s[0:1]
	s_mov_b32 s0, 0xfff00000
	s_mov_b32 s1, -1
	v_cmp_gt_u64_e32 vcc, s[0:1], v[20:21]
	v_mov_b64_e32 v[28:29], s[4:5]
	v_mov_b64_e32 v[30:31], s[8:9]
	s_and_saveexec_b64 s[0:1], vcc
	s_cbranch_execz .LBB0_22
	v_alignbit_b32 v32, v21, v20, 17
	v_cmp_lt_i32_e32 vcc, 0, v32
	s_mov_b64 s[2:3], 0
	s_and_saveexec_b64 s[4:5], vcc
	s_xor_b64 s[4:5], exec, s[4:5]
	s_cbranch_execz .LBB0_33
	v_cmp_eq_u32_e32 vcc, 1, v32
	s_mov_b64 s[2:3], -1
	s_and_saveexec_b64 s[6:7], vcc
	s_xor_b64 s[2:3], exec, -1
	s_or_b64 exec, exec, s[6:7]
	s_and_b64 s[2:3], s[2:3], exec
	s_or_saveexec_b64 s[4:5], s[4:5]
	v_mov_b64_e32 v[28:29], s[18:19]
	s_xor_b64 exec, exec, s[4:5]
	s_cbranch_execnz .LBB0_34

.LBB0_22:
	s_or_b64 exec, exec, s[0:1]
	v_lshlrev_b64 v[20:21], 5, v[26:27]
	v_lshl_add_u64 v[20:21], v[28:29], 0, v[20:21]
	global_load_dwordx4 v[32:35], v[20:21], off nt sc1
	global_load_dwordx4 v[36:39], v[20:21], off offset:16 nt sc1
	s_waitcnt vmcnt(4)
	v_cvt_pk_f16_f32 v4, v4, v5
	v_cvt_pk_f16_f32 v5, v6, v7
	v_cvt_pk_f16_f32 v6, v0, v1
	v_cvt_pk_f16_f32 v7, v2, v3
	v_lshl_add_u64 v[16:17], v[16:17], 4, v[18:19]
	s_waitcnt vmcnt(2)
	v_cvt_pk_f16_f32 v0, v12, v13
	v_cvt_pk_f16_f32 v1, v14, v15
	v_cvt_pk_f16_f32 v2, v8, v9
	v_cvt_pk_f16_f32 v3, v10, v11
	v_lshl_add_u64 v[8:9], v[22:23], 4, v[24:25]
	global_store_dwordx4 v[16:17], v[4:7], off sc0 sc1
	global_store_dwordx4 v[8:9], v[0:3], off sc0 sc1
	s_nop 0
	v_lshl_add_u64 v[4:5], v[26:27], 4, v[30:31]
	s_waitcnt vmcnt(3)
	v_cvt_pk_f16_f32 v0, v32, v33
	v_cvt_pk_f16_f32 v1, v34, v35
	s_waitcnt vmcnt(2)
	v_cvt_pk_f16_f32 v2, v36, v37
	v_cvt_pk_f16_f32 v3, v38, v39
	global_store_dwordx4 v[4:5], v[0:3], off sc0 sc1
	s_endpgm
